# static priority: waves 4-7 (trailing half) raised to priority 1 once at entry, all per-segment s_setprio toggles removed
# baseline (speedup 1.0000x reference)
; __device__ __forceinline__ int pg8_lane_id() { int l; asm volatile("v_mbcnt_lo_u32_b32 %0, -1, 0\n\tv_mbcnt_hi_u32_b32 %0, -1, %0" : "=v"(l)); return l; }
; #define LAS __attribute__((address_space(3)))
; __global__ void __launch_bounds__(NWAVES * 64, 2) mk_fwd(Args args) {
;     ...
;     F.wave = __builtin_amdgcn_readfirstlane((int)threadIdx.x >> 6);
;     F.G = gridDim.x; { const int bx = blockIdx.x; F.vcu = (F.G % 8 == 0) ? (bx % 8) * (F.G / 8) + bx / 8 : bx; F.c = bx; F.loc = 0; }
;     F.ws = args.ws; F.ctl = (gu32*)(args.ws + WS_CTL);
;     for (int u = F.wave * 64 + pg8::pg8_lane_id(); u < (LDS_BYTES - LDSCTL_OFF) / 4; u += NWAVES * 64) ((LAS unsigned*)(F.lds + LDSCTL_OFF))[u] = 0u;
;     __syncthreads();
.LBB0_2:
	s_and_b32 s3, s94, 0xffffffc0
	v_mbcnt_lo_u32_b32 v1, -1, 0
	v_mbcnt_hi_u32_b32 v1, -1, v1
	v_writelane_b32 v254, s3, 2
	v_add_u32_e32 v0, s3, v1
	s_movk_i32 s3, 0x1000
	s_lshr_b32 s96, s94, 6
	s_cmp_gt_u32 s96, 3
	s_cbranch_scc0 .Lmy_lowprio
	s_setprio 1
.Lmy_lowprio:
	v_cmp_gt_i32_e32 vcc, s3, v0
	s_and_saveexec_b64 s[4:5], vcc
	s_cbranch_execz .LBB0_5
	s_lshl_b32 s3, s96, 8
	s_add_i32 s3, s3, 0
	v_lshl_add_u32 v1, v1, 2, s3
	v_add_u32_e32 v0, 0xfffffe00, v0
	v_add_u32_e32 v1, 0x20000, v1
	s_mov_b64 s[6:7], 0
	v_mov_b32_e32 v2, 0
	s_movk_i32 s3, 0xdff
